# v87 + routing top-8 rounds: 64 DPP max steps fused into single v_max_f32_dpp instructions
# baseline (speedup 1.0000x reference)
.LBB0_585:
	s_or_b64 exec, exec, s[28:29]
	v_cmp_gt_f32_e32 vcc, v9, v20
	v_cndmask_b32_e64 v18, 0, 1, s[2:3]
	s_mov_b32 s2, 0xff800000
	v_cndmask_b32_e64 v9, 0, 1, vcc
	v_cmp_gt_f32_e32 vcc, v38, v20
	s_nop 1
	v_addc_co_u32_e32 v9, vcc, v9, v18, vcc
	v_cmp_gt_f32_e32 vcc, v0, v20
	s_nop 1
	v_cndmask_b32_e64 v0, 0, 1, vcc
	v_cmp_gt_f32_e32 vcc, v37, v20
	s_nop 1
	v_addc_co_u32_e32 v0, vcc, v9, v0, vcc
	v_cmp_gt_f32_e32 vcc, v39, v20
	s_nop 1
	v_cndmask_b32_e64 v9, 0, 1, vcc
	v_cmp_gt_f32_e32 vcc, v21, v20
	s_nop 1
	v_addc_co_u32_e32 v9, vcc, v0, v9, vcc
	v_mov_b32_e32 v0, s2
	v_cmp_gt_u32_e32 vcc, 4, v9
	s_nop 1
	v_cndmask_b32_e32 v9, v0, v14, vcc
	v_cndmask_b32_e32 v0, v17, v17, vcc
	v_cndmask_b32_e32 v16, v16, v16, vcc
	v_cndmask_b32_e32 v14, v15, v15, vcc
	v_cmp_gt_u32_e32 vcc, 4, v36
	s_nop 1
	v_cndmask_b32_e32 v14, v26, v14, vcc
	v_cmp_gt_u32_e32 vcc, 4, v35
	s_nop 1
	v_cndmask_b32_e32 v15, v26, v16, vcc
	v_cmp_gt_u32_e32 vcc, 4, v33
	v_max_f32_e32 v17, v15, v15
	s_nop 0
	v_cndmask_b32_e32 v0, v26, v0, vcc
	v_max_f32_e32 v16, v0, v0
	v_max_f32_e32 v16, v17, v16
	v_max3_f32 v16, v9, v14, v16
	s_nop 1
	v_max_f32_dpp v16, v16, v16 quad_perm:[1,0,3,2] row_mask:0xf bank_mask:0xf bound_ctrl:1
	s_nop 1
	v_max_f32_dpp v16, v16, v16 quad_perm:[2,3,0,1] row_mask:0xf bank_mask:0xf bound_ctrl:1
	s_nop 1
	v_max_f32_dpp v16, v16, v16 row_half_mirror row_mask:0xf bank_mask:0xf bound_ctrl:1
	s_nop 1
	v_max_f32_dpp v16, v16, v16 row_mirror row_mask:0xf bank_mask:0xf bound_ctrl:1
	v_mov_b32_e32 v17, v16
	v_mov_b32_e32 v60, v16
	s_nop 1
	v_permlane16_swap_b32 v17, v60
	v_max_f32_e32 v16, v17, v60
	v_mov_b32_e32 v17, v16
	v_mov_b32_e32 v60, v16
	s_nop 1
	v_permlane32_swap_b32 v17, v60
	v_max_f32_e32 v16, v17, v60
	v_cmp_eq_f32_e32 vcc, v9, v16
	v_cmp_eq_f32_e64 s[28:29], v14, v16
	v_cmp_eq_f32_e64 s[2:3], v15, v16
	v_cmp_eq_f32_e64 s[48:49], v0, v16
	s_cbranch_vccz .LBB0_587
	s_ff1_i32_b64 s56, vcc
	s_cbranch_execz .LBB0_588
	s_branch .LBB0_594

.LBB0_594:
	s_and_b32 s2, s56, 63
	s_lshr_b32 s28, s56, 6
	s_cmp_lt_u32 s56, 64
	v_cmp_eq_u32_e32 vcc, s2, v22
	s_cselect_b64 s[2:3], -1, 0
	s_and_b64 s[2:3], s[2:3], vcc
	s_cmp_eq_u32 s28, 1
	v_cndmask_b32_e64 v9, v9, v26, s[2:3]
	s_cselect_b64 s[2:3], -1, 0
	s_and_b64 s[2:3], vcc, s[2:3]
	s_cmp_eq_u32 s28, 2
	v_cndmask_b32_e64 v14, v14, v26, s[2:3]
	s_cselect_b64 s[2:3], -1, 0
	s_and_b64 s[2:3], vcc, s[2:3]
	s_cmp_eq_u32 s28, 3
	v_cndmask_b32_e64 v15, v15, v26, s[2:3]
	s_cselect_b64 s[2:3], -1, 0
	s_and_b64 vcc, vcc, s[2:3]
	v_cndmask_b32_e32 v0, v0, v26, vcc
	v_max_f32_e32 v16, v0, v0
	v_max_f32_e32 v17, v15, v15
	v_max_f32_e32 v16, v17, v16
	v_max3_f32 v16, v9, v14, v16
	s_nop 1
	v_max_f32_dpp v16, v16, v16 quad_perm:[1,0,3,2] row_mask:0xf bank_mask:0xf bound_ctrl:1
	s_nop 1
	v_max_f32_dpp v16, v16, v16 quad_perm:[2,3,0,1] row_mask:0xf bank_mask:0xf bound_ctrl:1
	s_nop 1
	v_max_f32_dpp v16, v16, v16 row_half_mirror row_mask:0xf bank_mask:0xf bound_ctrl:1
	s_nop 1
	v_max_f32_dpp v16, v16, v16 row_mirror row_mask:0xf bank_mask:0xf bound_ctrl:1
	v_mov_b32_e32 v17, v16
	v_mov_b32_e32 v60, v16
	s_nop 1
	v_permlane16_swap_b32 v17, v60
	v_max_f32_e32 v16, v17, v60
	v_mov_b32_e32 v17, v16
	v_mov_b32_e32 v60, v16
	s_nop 1
	v_permlane32_swap_b32 v17, v60
	v_max_f32_e32 v16, v17, v60
	v_cmp_eq_f32_e32 vcc, v9, v16
	v_cmp_eq_f32_e64 s[28:29], v14, v16
	v_cmp_eq_f32_e64 s[2:3], v15, v16
	v_cmp_eq_f32_e64 s[48:49], v0, v16
	s_cbranch_vccz .LBB0_596
	s_ff1_i32_b64 s57, vcc
	s_cbranch_execz .LBB0_597
	s_branch .LBB0_603

.LBB0_603:
	s_and_b32 s2, s57, 63
	s_lshr_b32 s28, s57, 6
	s_cmp_lt_u32 s57, 64
	v_cmp_eq_u32_e32 vcc, s2, v22
	s_cselect_b64 s[2:3], -1, 0
	s_and_b64 s[2:3], s[2:3], vcc
	s_cmp_eq_u32 s28, 1
	v_cndmask_b32_e64 v9, v9, v26, s[2:3]
	s_cselect_b64 s[2:3], -1, 0
	s_and_b64 s[2:3], vcc, s[2:3]
	s_cmp_eq_u32 s28, 2
	v_cndmask_b32_e64 v14, v14, v26, s[2:3]
	s_cselect_b64 s[2:3], -1, 0
	s_and_b64 s[2:3], vcc, s[2:3]
	s_cmp_eq_u32 s28, 3
	v_cndmask_b32_e64 v15, v15, v26, s[2:3]
	s_cselect_b64 s[2:3], -1, 0
	s_and_b64 vcc, vcc, s[2:3]
	v_cndmask_b32_e32 v0, v0, v26, vcc
	v_max_f32_e32 v16, v0, v0
	v_max_f32_e32 v17, v15, v15
	v_max_f32_e32 v16, v17, v16
	v_max3_f32 v16, v9, v14, v16
	s_nop 1
	v_max_f32_dpp v16, v16, v16 quad_perm:[1,0,3,2] row_mask:0xf bank_mask:0xf bound_ctrl:1
	s_nop 1
	v_max_f32_dpp v16, v16, v16 quad_perm:[2,3,0,1] row_mask:0xf bank_mask:0xf bound_ctrl:1
	s_nop 1
	v_max_f32_dpp v16, v16, v16 row_half_mirror row_mask:0xf bank_mask:0xf bound_ctrl:1
	s_nop 1
	v_max_f32_dpp v16, v16, v16 row_mirror row_mask:0xf bank_mask:0xf bound_ctrl:1
	v_mov_b32_e32 v17, v16
	v_mov_b32_e32 v60, v16
	s_nop 1
	v_permlane16_swap_b32 v17, v60
	v_max_f32_e32 v16, v17, v60
	v_mov_b32_e32 v17, v16
	v_mov_b32_e32 v60, v16
	s_nop 1
	v_permlane32_swap_b32 v17, v60
	v_max_f32_e32 v16, v17, v60
	v_cmp_eq_f32_e32 vcc, v9, v16
	v_cmp_eq_f32_e64 s[28:29], v14, v16
	v_cmp_eq_f32_e64 s[2:3], v15, v16
	v_cmp_eq_f32_e64 s[48:49], v0, v16
	s_cbranch_vccz .LBB0_605
	s_ff1_i32_b64 s58, vcc
	s_cbranch_execz .LBB0_606
	s_branch .LBB0_612

.LBB0_612:
	s_and_b32 s2, s58, 63
	s_lshr_b32 s28, s58, 6
	s_cmp_lt_u32 s58, 64
	v_cmp_eq_u32_e32 vcc, s2, v22
	s_cselect_b64 s[2:3], -1, 0
	s_and_b64 s[2:3], s[2:3], vcc
	s_cmp_eq_u32 s28, 1
	v_cndmask_b32_e64 v9, v9, v26, s[2:3]
	s_cselect_b64 s[2:3], -1, 0
	s_and_b64 s[2:3], vcc, s[2:3]
	s_cmp_eq_u32 s28, 2
	v_cndmask_b32_e64 v14, v14, v26, s[2:3]
	s_cselect_b64 s[2:3], -1, 0
	s_and_b64 s[2:3], vcc, s[2:3]
	s_cmp_eq_u32 s28, 3
	v_cndmask_b32_e64 v15, v15, v26, s[2:3]
	s_cselect_b64 s[2:3], -1, 0
	s_and_b64 vcc, vcc, s[2:3]
	v_cndmask_b32_e32 v0, v0, v26, vcc
	v_max_f32_e32 v16, v0, v0
	v_max_f32_e32 v17, v15, v15
	v_max_f32_e32 v16, v17, v16
	v_max3_f32 v16, v9, v14, v16
	s_nop 1
	v_max_f32_dpp v16, v16, v16 quad_perm:[1,0,3,2] row_mask:0xf bank_mask:0xf bound_ctrl:1
	s_nop 1
	v_max_f32_dpp v16, v16, v16 quad_perm:[2,3,0,1] row_mask:0xf bank_mask:0xf bound_ctrl:1
	s_nop 1
	v_max_f32_dpp v16, v16, v16 row_half_mirror row_mask:0xf bank_mask:0xf bound_ctrl:1
	s_nop 1
	v_max_f32_dpp v16, v16, v16 row_mirror row_mask:0xf bank_mask:0xf bound_ctrl:1
	v_mov_b32_e32 v17, v16
	v_mov_b32_e32 v60, v16
	s_nop 1
	v_permlane16_swap_b32 v17, v60
	v_max_f32_e32 v16, v17, v60
	v_mov_b32_e32 v17, v16
	v_mov_b32_e32 v60, v16
	s_nop 1
	v_permlane32_swap_b32 v17, v60
	v_max_f32_e32 v16, v17, v60
	v_cmp_eq_f32_e32 vcc, v9, v16
	v_cmp_eq_f32_e64 s[28:29], v14, v16
	v_cmp_eq_f32_e64 s[2:3], v15, v16
	v_cmp_eq_f32_e64 s[48:49], v0, v16
	s_cbranch_vccz .LBB0_614
	s_ff1_i32_b64 s59, vcc
	s_cbranch_execz .LBB0_615
	s_branch .LBB0_621

.LBB0_621:
	s_and_b32 s2, s59, 63
	s_lshr_b32 s28, s59, 6
	s_cmp_lt_u32 s59, 64
	v_cmp_eq_u32_e32 vcc, s2, v22
	s_cselect_b64 s[2:3], -1, 0
	s_and_b64 s[2:3], s[2:3], vcc
	s_cmp_eq_u32 s28, 1
	v_cndmask_b32_e64 v9, v9, v26, s[2:3]
	s_cselect_b64 s[2:3], -1, 0
	s_and_b64 s[2:3], vcc, s[2:3]
	s_cmp_eq_u32 s28, 2
	v_cndmask_b32_e64 v14, v14, v26, s[2:3]
	s_cselect_b64 s[2:3], -1, 0
	s_and_b64 s[2:3], vcc, s[2:3]
	s_cmp_eq_u32 s28, 3
	v_cndmask_b32_e64 v15, v15, v26, s[2:3]
	s_cselect_b64 s[2:3], -1, 0
	s_and_b64 vcc, vcc, s[2:3]
	v_cndmask_b32_e32 v0, v0, v26, vcc
	v_max_f32_e32 v16, v0, v0
	v_max_f32_e32 v17, v15, v15
	v_max_f32_e32 v16, v17, v16
	v_max3_f32 v16, v9, v14, v16
	s_nop 1
	v_max_f32_dpp v16, v16, v16 quad_perm:[1,0,3,2] row_mask:0xf bank_mask:0xf bound_ctrl:1
	s_nop 1
	v_max_f32_dpp v16, v16, v16 quad_perm:[2,3,0,1] row_mask:0xf bank_mask:0xf bound_ctrl:1
	s_nop 1
	v_max_f32_dpp v16, v16, v16 row_half_mirror row_mask:0xf bank_mask:0xf bound_ctrl:1
	s_nop 1
	v_max_f32_dpp v16, v16, v16 row_mirror row_mask:0xf bank_mask:0xf bound_ctrl:1
	v_mov_b32_e32 v17, v16
	v_mov_b32_e32 v60, v16
	s_nop 1
	v_permlane16_swap_b32 v17, v60
	v_max_f32_e32 v16, v17, v60
	v_mov_b32_e32 v17, v16
	v_mov_b32_e32 v60, v16
	s_nop 1
	v_permlane32_swap_b32 v17, v60
	v_max_f32_e32 v16, v17, v60
	v_cmp_eq_f32_e32 vcc, v9, v16
	v_cmp_eq_f32_e64 s[28:29], v14, v16
	v_cmp_eq_f32_e64 s[2:3], v15, v16
	v_cmp_eq_f32_e64 s[48:49], v0, v16
	s_cbranch_vccz .LBB0_623
	s_ff1_i32_b64 s60, vcc
	s_cbranch_execz .LBB0_624
	s_branch .LBB0_630

.LBB0_630:
	s_and_b32 s2, s60, 63
	s_lshr_b32 s28, s60, 6
	s_cmp_lt_u32 s60, 64
	v_cmp_eq_u32_e32 vcc, s2, v22
	s_cselect_b64 s[2:3], -1, 0
	s_and_b64 s[2:3], s[2:3], vcc
	s_cmp_eq_u32 s28, 1
	v_cndmask_b32_e64 v9, v9, v26, s[2:3]
	s_cselect_b64 s[2:3], -1, 0
	s_and_b64 s[2:3], vcc, s[2:3]
	s_cmp_eq_u32 s28, 2
	v_cndmask_b32_e64 v14, v14, v26, s[2:3]
	s_cselect_b64 s[2:3], -1, 0
	s_and_b64 s[2:3], vcc, s[2:3]
	s_cmp_eq_u32 s28, 3
	v_cndmask_b32_e64 v15, v15, v26, s[2:3]
	s_cselect_b64 s[2:3], -1, 0
	s_and_b64 vcc, vcc, s[2:3]
	v_cndmask_b32_e32 v0, v0, v26, vcc
	v_max_f32_e32 v16, v0, v0
	v_max_f32_e32 v17, v15, v15
	v_max_f32_e32 v16, v17, v16
	v_max3_f32 v16, v9, v14, v16
	s_nop 1
	v_max_f32_dpp v16, v16, v16 quad_perm:[1,0,3,2] row_mask:0xf bank_mask:0xf bound_ctrl:1
	s_nop 1
	v_max_f32_dpp v16, v16, v16 quad_perm:[2,3,0,1] row_mask:0xf bank_mask:0xf bound_ctrl:1
	s_nop 1
	v_max_f32_dpp v16, v16, v16 row_half_mirror row_mask:0xf bank_mask:0xf bound_ctrl:1
	s_nop 1
	v_max_f32_dpp v16, v16, v16 row_mirror row_mask:0xf bank_mask:0xf bound_ctrl:1
	v_mov_b32_e32 v17, v16
	v_mov_b32_e32 v60, v16
	s_nop 1
	v_permlane16_swap_b32 v17, v60
	v_max_f32_e32 v16, v17, v60
	v_mov_b32_e32 v17, v16
	v_mov_b32_e32 v60, v16
	s_nop 1
	v_permlane32_swap_b32 v17, v60
	v_max_f32_e32 v16, v17, v60
	v_cmp_eq_f32_e32 vcc, v9, v16
	v_cmp_eq_f32_e64 s[28:29], v14, v16
	v_cmp_eq_f32_e64 s[2:3], v15, v16
	v_cmp_eq_f32_e64 s[48:49], v0, v16
	s_cbranch_vccz .LBB0_632
	s_ff1_i32_b64 s61, vcc
	s_cbranch_execz .LBB0_633
	s_branch .LBB0_639

.LBB0_639:
	s_and_b32 s2, s61, 63
	s_lshr_b32 s28, s61, 6
	s_cmp_lt_u32 s61, 64
	v_cmp_eq_u32_e32 vcc, s2, v22
	s_cselect_b64 s[2:3], -1, 0
	s_and_b64 s[2:3], s[2:3], vcc
	s_cmp_eq_u32 s28, 1
	v_cndmask_b32_e64 v9, v9, v26, s[2:3]
	s_cselect_b64 s[2:3], -1, 0
	s_and_b64 s[2:3], vcc, s[2:3]
	s_cmp_eq_u32 s28, 2
	v_cndmask_b32_e64 v14, v14, v26, s[2:3]
	s_cselect_b64 s[2:3], -1, 0
	s_and_b64 s[2:3], vcc, s[2:3]
	s_cmp_eq_u32 s28, 3
	v_cndmask_b32_e64 v15, v15, v26, s[2:3]
	s_cselect_b64 s[2:3], -1, 0
	s_and_b64 vcc, vcc, s[2:3]
	v_cndmask_b32_e32 v0, v0, v26, vcc
	v_max_f32_e32 v16, v0, v0
	v_max_f32_e32 v17, v15, v15
	v_max_f32_e32 v16, v17, v16
	v_max3_f32 v16, v9, v14, v16
	s_nop 1
	v_max_f32_dpp v16, v16, v16 quad_perm:[1,0,3,2] row_mask:0xf bank_mask:0xf bound_ctrl:1
	s_nop 1
	v_max_f32_dpp v16, v16, v16 quad_perm:[2,3,0,1] row_mask:0xf bank_mask:0xf bound_ctrl:1
	s_nop 1
	v_max_f32_dpp v16, v16, v16 row_half_mirror row_mask:0xf bank_mask:0xf bound_ctrl:1
	s_nop 1
	v_max_f32_dpp v16, v16, v16 row_mirror row_mask:0xf bank_mask:0xf bound_ctrl:1
	v_mov_b32_e32 v17, v16
	v_mov_b32_e32 v60, v16
	s_nop 1
	v_permlane16_swap_b32 v17, v60
	v_max_f32_e32 v16, v17, v60
	v_mov_b32_e32 v17, v16
	v_mov_b32_e32 v60, v16
	s_nop 1
	v_permlane32_swap_b32 v17, v60
	v_max_f32_e32 v16, v17, v60
	v_cmp_eq_f32_e32 vcc, v9, v16
	v_cmp_eq_f32_e64 s[28:29], v14, v16
	v_cmp_eq_f32_e64 s[2:3], v15, v16
	v_cmp_eq_f32_e64 s[48:49], v0, v16
	s_cbranch_vccz .LBB0_641
	s_ff1_i32_b64 s62, vcc
	s_cbranch_execz .LBB0_642
	s_branch .LBB0_648

.LBB0_648:
	s_and_b32 s2, s62, 63
	s_lshr_b32 s28, s62, 6
	s_cmp_lt_u32 s62, 64
	v_cmp_eq_u32_e32 vcc, s2, v22
	s_cselect_b64 s[2:3], -1, 0
	s_and_b64 s[2:3], s[2:3], vcc
	s_cmp_eq_u32 s28, 1
	v_cndmask_b32_e64 v9, v9, v26, s[2:3]
	s_cselect_b64 s[2:3], -1, 0
	s_and_b64 s[2:3], vcc, s[2:3]
	s_cmp_eq_u32 s28, 2
	v_cndmask_b32_e64 v14, v14, v26, s[2:3]
	s_cselect_b64 s[2:3], -1, 0
	s_and_b64 s[2:3], vcc, s[2:3]
	s_cmp_eq_u32 s28, 3
	v_cndmask_b32_e64 v15, v15, v26, s[2:3]
	s_cselect_b64 s[2:3], -1, 0
	s_and_b64 vcc, vcc, s[2:3]
	v_cndmask_b32_e32 v0, v0, v26, vcc
	v_max_f32_e32 v16, v0, v0
	v_max_f32_e32 v17, v15, v15
	v_max_f32_e32 v16, v17, v16
	v_max3_f32 v16, v9, v14, v16
	s_nop 1
	v_max_f32_dpp v16, v16, v16 quad_perm:[1,0,3,2] row_mask:0xf bank_mask:0xf bound_ctrl:1
	s_nop 1
	v_max_f32_dpp v16, v16, v16 quad_perm:[2,3,0,1] row_mask:0xf bank_mask:0xf bound_ctrl:1
	s_nop 1
	v_max_f32_dpp v16, v16, v16 row_half_mirror row_mask:0xf bank_mask:0xf bound_ctrl:1
	s_nop 1
	v_max_f32_dpp v16, v16, v16 row_mirror row_mask:0xf bank_mask:0xf bound_ctrl:1
	v_mov_b32_e32 v17, v16
	v_mov_b32_e32 v60, v16
	s_nop 1
	v_permlane16_swap_b32 v17, v60
	v_max_f32_e32 v16, v17, v60
	v_mov_b32_e32 v17, v16
	v_mov_b32_e32 v60, v16
	s_nop 1
	v_permlane32_swap_b32 v17, v60
	v_max_f32_e32 v16, v17, v60
	v_cmp_eq_f32_e32 vcc, v9, v16
	v_cmp_eq_f32_e64 s[28:29], v14, v16
	v_cmp_eq_f32_e64 s[2:3], v15, v16
	v_cmp_eq_f32_e64 s[48:49], v0, v16
	s_cbranch_vccz .LBB0_650
	s_ff1_i32_b64 s63, vcc
	s_cbranch_execz .LBB0_651
	s_branch .LBB0_657

.LBB0_2167:
	s_or_b64 exec, exec, s[28:29]
	v_cmp_gt_f32_e32 vcc, v0, v20
	v_cndmask_b32_e64 v18, 0, 1, s[26:27]
	s_nop 0
	v_cndmask_b32_e64 v0, 0, 1, vcc
	v_cmp_gt_f32_e32 vcc, v38, v20
	s_nop 1
	v_addc_co_u32_e32 v0, vcc, v0, v18, vcc
	v_cmp_gt_f32_e32 vcc, v9, v20
	s_nop 1
	v_cndmask_b32_e64 v9, 0, 1, vcc
	v_cmp_gt_f32_e32 vcc, v37, v20
	s_nop 1
	v_addc_co_u32_e32 v0, vcc, v0, v9, vcc
	v_cmp_gt_f32_e32 vcc, v39, v20
	s_nop 1
	v_cndmask_b32_e64 v9, 0, 1, vcc
	v_cmp_gt_f32_e32 vcc, v21, v20
	s_nop 1
	v_addc_co_u32_e32 v9, vcc, v0, v9, vcc
	v_mov_b32_e32 v0, s47
	v_cmp_gt_u32_e32 vcc, 4, v9
	s_nop 1
	v_cndmask_b32_e32 v9, v0, v14, vcc
	v_cndmask_b32_e32 v0, v17, v17, vcc
	v_cndmask_b32_e32 v16, v16, v16, vcc
	v_cndmask_b32_e32 v14, v15, v15, vcc
	v_cmp_gt_u32_e32 vcc, 4, v35
	s_nop 1
	v_cndmask_b32_e32 v14, v25, v14, vcc
	v_cmp_gt_u32_e32 vcc, 4, v34
	s_nop 1
	v_cndmask_b32_e32 v15, v25, v16, vcc
	v_cmp_gt_u32_e32 vcc, 4, v33
	v_max_f32_e32 v17, v15, v15
	s_nop 0
	v_cndmask_b32_e32 v0, v25, v0, vcc
	v_max_f32_e32 v16, v0, v0
	v_max_f32_e32 v16, v17, v16
	v_max3_f32 v16, v9, v14, v16
	s_nop 1
	v_max_f32_dpp v16, v16, v16 quad_perm:[1,0,3,2] row_mask:0xf bank_mask:0xf bound_ctrl:1
	s_nop 1
	v_max_f32_dpp v16, v16, v16 quad_perm:[2,3,0,1] row_mask:0xf bank_mask:0xf bound_ctrl:1
	s_nop 1
	v_max_f32_dpp v16, v16, v16 row_half_mirror row_mask:0xf bank_mask:0xf bound_ctrl:1
	s_nop 1
	v_max_f32_dpp v16, v16, v16 row_mirror row_mask:0xf bank_mask:0xf bound_ctrl:1
	v_mov_b32_e32 v17, v16
	v_mov_b32_e32 v60, v16
	s_nop 1
	v_permlane16_swap_b32 v17, v60
	v_max_f32_e32 v16, v17, v60
	v_mov_b32_e32 v17, v16
	v_mov_b32_e32 v60, v16
	s_nop 1
	v_permlane32_swap_b32 v17, v60
	v_max_f32_e32 v16, v17, v60
	v_cmp_eq_f32_e32 vcc, v9, v16
	v_cmp_eq_f32_e64 s[28:29], v14, v16
	v_cmp_eq_f32_e64 s[26:27], v15, v16
	v_cmp_eq_f32_e64 s[38:39], v0, v16
	s_cbranch_vccz .LBB0_2169
	s_ff1_i32_b64 s48, vcc
	s_cbranch_execz .LBB0_2170
	s_branch .LBB0_2176

.LBB0_2176:
	s_and_b32 s26, s48, 63
	s_lshr_b32 s28, s48, 6
	s_cmp_lt_u32 s48, 64
	v_cmp_eq_u32_e32 vcc, s26, v22
	s_cselect_b64 s[26:27], -1, 0
	s_and_b64 s[26:27], s[26:27], vcc
	s_cmp_eq_u32 s28, 1
	v_cndmask_b32_e64 v9, v9, v25, s[26:27]
	s_cselect_b64 s[26:27], -1, 0
	s_and_b64 s[26:27], vcc, s[26:27]
	s_cmp_eq_u32 s28, 2
	v_cndmask_b32_e64 v14, v14, v25, s[26:27]
	s_cselect_b64 s[26:27], -1, 0
	s_and_b64 s[26:27], vcc, s[26:27]
	s_cmp_eq_u32 s28, 3
	v_cndmask_b32_e64 v15, v15, v25, s[26:27]
	s_cselect_b64 s[26:27], -1, 0
	s_and_b64 vcc, vcc, s[26:27]
	v_cndmask_b32_e32 v0, v0, v25, vcc
	v_max_f32_e32 v16, v0, v0
	v_max_f32_e32 v17, v15, v15
	v_max_f32_e32 v16, v17, v16
	v_max3_f32 v16, v9, v14, v16
	s_nop 1
	v_max_f32_dpp v16, v16, v16 quad_perm:[1,0,3,2] row_mask:0xf bank_mask:0xf bound_ctrl:1
	s_nop 1
	v_max_f32_dpp v16, v16, v16 quad_perm:[2,3,0,1] row_mask:0xf bank_mask:0xf bound_ctrl:1
	s_nop 1
	v_max_f32_dpp v16, v16, v16 row_half_mirror row_mask:0xf bank_mask:0xf bound_ctrl:1
	s_nop 1
	v_max_f32_dpp v16, v16, v16 row_mirror row_mask:0xf bank_mask:0xf bound_ctrl:1
	v_mov_b32_e32 v17, v16
	v_mov_b32_e32 v60, v16
	s_nop 1
	v_permlane16_swap_b32 v17, v60
	v_max_f32_e32 v16, v17, v60
	v_mov_b32_e32 v17, v16
	v_mov_b32_e32 v60, v16
	s_nop 1
	v_permlane32_swap_b32 v17, v60
	v_max_f32_e32 v16, v17, v60
	v_cmp_eq_f32_e32 vcc, v9, v16
	v_cmp_eq_f32_e64 s[28:29], v14, v16
	v_cmp_eq_f32_e64 s[26:27], v15, v16
	v_cmp_eq_f32_e64 s[38:39], v0, v16
	s_cbranch_vccz .LBB0_2178
	s_ff1_i32_b64 s49, vcc
	s_cbranch_execz .LBB0_2179
	s_branch .LBB0_2185

.LBB0_2185:
	s_and_b32 s26, s49, 63
	s_lshr_b32 s28, s49, 6
	s_cmp_lt_u32 s49, 64
	v_cmp_eq_u32_e32 vcc, s26, v22
	s_cselect_b64 s[26:27], -1, 0
	s_and_b64 s[26:27], s[26:27], vcc
	s_cmp_eq_u32 s28, 1
	v_cndmask_b32_e64 v9, v9, v25, s[26:27]
	s_cselect_b64 s[26:27], -1, 0
	s_and_b64 s[26:27], vcc, s[26:27]
	s_cmp_eq_u32 s28, 2
	v_cndmask_b32_e64 v14, v14, v25, s[26:27]
	s_cselect_b64 s[26:27], -1, 0
	s_and_b64 s[26:27], vcc, s[26:27]
	s_cmp_eq_u32 s28, 3
	v_cndmask_b32_e64 v15, v15, v25, s[26:27]
	s_cselect_b64 s[26:27], -1, 0
	s_and_b64 vcc, vcc, s[26:27]
	v_cndmask_b32_e32 v0, v0, v25, vcc
	v_max_f32_e32 v16, v0, v0
	v_max_f32_e32 v17, v15, v15
	v_max_f32_e32 v16, v17, v16
	v_max3_f32 v16, v9, v14, v16
	s_nop 1
	v_max_f32_dpp v16, v16, v16 quad_perm:[1,0,3,2] row_mask:0xf bank_mask:0xf bound_ctrl:1
	s_nop 1
	v_max_f32_dpp v16, v16, v16 quad_perm:[2,3,0,1] row_mask:0xf bank_mask:0xf bound_ctrl:1
	s_nop 1
	v_max_f32_dpp v16, v16, v16 row_half_mirror row_mask:0xf bank_mask:0xf bound_ctrl:1
	s_nop 1
	v_max_f32_dpp v16, v16, v16 row_mirror row_mask:0xf bank_mask:0xf bound_ctrl:1
	v_mov_b32_e32 v17, v16
	v_mov_b32_e32 v60, v16
	s_nop 1
	v_permlane16_swap_b32 v17, v60
	v_max_f32_e32 v16, v17, v60
	v_mov_b32_e32 v17, v16
	v_mov_b32_e32 v60, v16
	s_nop 1
	v_permlane32_swap_b32 v17, v60
	v_max_f32_e32 v16, v17, v60
	v_cmp_eq_f32_e32 vcc, v9, v16
	v_cmp_eq_f32_e64 s[28:29], v14, v16
	v_cmp_eq_f32_e64 s[26:27], v15, v16
	v_cmp_eq_f32_e64 s[38:39], v0, v16
	s_cbranch_vccz .LBB0_2187
	s_ff1_i32_b64 s50, vcc
	s_cbranch_execz .LBB0_2188
	s_branch .LBB0_2194

.LBB0_2194:
	s_and_b32 s26, s50, 63
	s_lshr_b32 s28, s50, 6
	s_cmp_lt_u32 s50, 64
	v_cmp_eq_u32_e32 vcc, s26, v22
	s_cselect_b64 s[26:27], -1, 0
	s_and_b64 s[26:27], s[26:27], vcc
	s_cmp_eq_u32 s28, 1
	v_cndmask_b32_e64 v9, v9, v25, s[26:27]
	s_cselect_b64 s[26:27], -1, 0
	s_and_b64 s[26:27], vcc, s[26:27]
	s_cmp_eq_u32 s28, 2
	v_cndmask_b32_e64 v14, v14, v25, s[26:27]
	s_cselect_b64 s[26:27], -1, 0
	s_and_b64 s[26:27], vcc, s[26:27]
	s_cmp_eq_u32 s28, 3
	v_cndmask_b32_e64 v15, v15, v25, s[26:27]
	s_cselect_b64 s[26:27], -1, 0
	s_and_b64 vcc, vcc, s[26:27]
	v_cndmask_b32_e32 v0, v0, v25, vcc
	v_max_f32_e32 v16, v0, v0
	v_max_f32_e32 v17, v15, v15
	v_max_f32_e32 v16, v17, v16
	v_max3_f32 v16, v9, v14, v16
	s_nop 1
	v_max_f32_dpp v16, v16, v16 quad_perm:[1,0,3,2] row_mask:0xf bank_mask:0xf bound_ctrl:1
	s_nop 1
	v_max_f32_dpp v16, v16, v16 quad_perm:[2,3,0,1] row_mask:0xf bank_mask:0xf bound_ctrl:1
	s_nop 1
	v_max_f32_dpp v16, v16, v16 row_half_mirror row_mask:0xf bank_mask:0xf bound_ctrl:1
	s_nop 1
	v_max_f32_dpp v16, v16, v16 row_mirror row_mask:0xf bank_mask:0xf bound_ctrl:1
	v_mov_b32_e32 v17, v16
	v_mov_b32_e32 v60, v16
	s_nop 1
	v_permlane16_swap_b32 v17, v60
	v_max_f32_e32 v16, v17, v60
	v_mov_b32_e32 v17, v16
	v_mov_b32_e32 v60, v16
	s_nop 1
	v_permlane32_swap_b32 v17, v60
	v_max_f32_e32 v16, v17, v60
	v_cmp_eq_f32_e32 vcc, v9, v16
	v_cmp_eq_f32_e64 s[28:29], v14, v16
	v_cmp_eq_f32_e64 s[26:27], v15, v16
	v_cmp_eq_f32_e64 s[38:39], v0, v16
	s_cbranch_vccz .LBB0_2196
	s_ff1_i32_b64 s51, vcc
	s_cbranch_execz .LBB0_2197
	s_branch .LBB0_2203

.LBB0_2203:
	s_and_b32 s26, s51, 63
	s_lshr_b32 s28, s51, 6
	s_cmp_lt_u32 s51, 64
	v_cmp_eq_u32_e32 vcc, s26, v22
	s_cselect_b64 s[26:27], -1, 0
	s_and_b64 s[26:27], s[26:27], vcc
	s_cmp_eq_u32 s28, 1
	v_cndmask_b32_e64 v9, v9, v25, s[26:27]
	s_cselect_b64 s[26:27], -1, 0
	s_and_b64 s[26:27], vcc, s[26:27]
	s_cmp_eq_u32 s28, 2
	v_cndmask_b32_e64 v14, v14, v25, s[26:27]
	s_cselect_b64 s[26:27], -1, 0
	s_and_b64 s[26:27], vcc, s[26:27]
	s_cmp_eq_u32 s28, 3
	v_cndmask_b32_e64 v15, v15, v25, s[26:27]
	s_cselect_b64 s[26:27], -1, 0
	s_and_b64 vcc, vcc, s[26:27]
	v_cndmask_b32_e32 v0, v0, v25, vcc
	v_max_f32_e32 v16, v0, v0
	v_max_f32_e32 v17, v15, v15
	v_max_f32_e32 v16, v17, v16
	v_max3_f32 v16, v9, v14, v16
	s_nop 1
	v_max_f32_dpp v16, v16, v16 quad_perm:[1,0,3,2] row_mask:0xf bank_mask:0xf bound_ctrl:1
	s_nop 1
	v_max_f32_dpp v16, v16, v16 quad_perm:[2,3,0,1] row_mask:0xf bank_mask:0xf bound_ctrl:1
	s_nop 1
	v_max_f32_dpp v16, v16, v16 row_half_mirror row_mask:0xf bank_mask:0xf bound_ctrl:1
	s_nop 1
	v_max_f32_dpp v16, v16, v16 row_mirror row_mask:0xf bank_mask:0xf bound_ctrl:1
	v_mov_b32_e32 v17, v16
	v_mov_b32_e32 v60, v16
	s_nop 1
	v_permlane16_swap_b32 v17, v60
	v_max_f32_e32 v16, v17, v60
	v_mov_b32_e32 v17, v16
	v_mov_b32_e32 v60, v16
	s_nop 1
	v_permlane32_swap_b32 v17, v60
	v_max_f32_e32 v16, v17, v60
	v_cmp_eq_f32_e32 vcc, v9, v16
	v_cmp_eq_f32_e64 s[28:29], v14, v16
	v_cmp_eq_f32_e64 s[26:27], v15, v16
	v_cmp_eq_f32_e64 s[38:39], v0, v16
	s_cbranch_vccz .LBB0_2205
	s_ff1_i32_b64 s52, vcc
	s_cbranch_execz .LBB0_2206
	s_branch .LBB0_2212

.LBB0_2212:
	s_and_b32 s26, s52, 63
	s_lshr_b32 s28, s52, 6
	s_cmp_lt_u32 s52, 64
	v_cmp_eq_u32_e32 vcc, s26, v22
	s_cselect_b64 s[26:27], -1, 0
	s_and_b64 s[26:27], s[26:27], vcc
	s_cmp_eq_u32 s28, 1
	v_cndmask_b32_e64 v9, v9, v25, s[26:27]
	s_cselect_b64 s[26:27], -1, 0
	s_and_b64 s[26:27], vcc, s[26:27]
	s_cmp_eq_u32 s28, 2
	v_cndmask_b32_e64 v14, v14, v25, s[26:27]
	s_cselect_b64 s[26:27], -1, 0
	s_and_b64 s[26:27], vcc, s[26:27]
	s_cmp_eq_u32 s28, 3
	v_cndmask_b32_e64 v15, v15, v25, s[26:27]
	s_cselect_b64 s[26:27], -1, 0
	s_and_b64 vcc, vcc, s[26:27]
	v_cndmask_b32_e32 v0, v0, v25, vcc
	v_max_f32_e32 v16, v0, v0
	v_max_f32_e32 v17, v15, v15
	v_max_f32_e32 v16, v17, v16
	v_max3_f32 v16, v9, v14, v16
	s_nop 1
	v_max_f32_dpp v16, v16, v16 quad_perm:[1,0,3,2] row_mask:0xf bank_mask:0xf bound_ctrl:1
	s_nop 1
	v_max_f32_dpp v16, v16, v16 quad_perm:[2,3,0,1] row_mask:0xf bank_mask:0xf bound_ctrl:1
	s_nop 1
	v_max_f32_dpp v16, v16, v16 row_half_mirror row_mask:0xf bank_mask:0xf bound_ctrl:1
	s_nop 1
	v_max_f32_dpp v16, v16, v16 row_mirror row_mask:0xf bank_mask:0xf bound_ctrl:1
	v_mov_b32_e32 v17, v16
	v_mov_b32_e32 v60, v16
	s_nop 1
	v_permlane16_swap_b32 v17, v60
	v_max_f32_e32 v16, v17, v60
	v_mov_b32_e32 v17, v16
	v_mov_b32_e32 v60, v16
	s_nop 1
	v_permlane32_swap_b32 v17, v60
	v_max_f32_e32 v16, v17, v60
	v_cmp_eq_f32_e32 vcc, v9, v16
	v_cmp_eq_f32_e64 s[28:29], v14, v16
	v_cmp_eq_f32_e64 s[26:27], v15, v16
	v_cmp_eq_f32_e64 s[38:39], v0, v16
	s_cbranch_vccz .LBB0_2214
	s_ff1_i32_b64 s53, vcc
	s_cbranch_execz .LBB0_2215
	s_branch .LBB0_2221

.LBB0_2221:
	s_and_b32 s26, s53, 63
	s_lshr_b32 s28, s53, 6
	s_cmp_lt_u32 s53, 64
	v_cmp_eq_u32_e32 vcc, s26, v22
	s_cselect_b64 s[26:27], -1, 0
	s_and_b64 s[26:27], s[26:27], vcc
	s_cmp_eq_u32 s28, 1
	v_cndmask_b32_e64 v9, v9, v25, s[26:27]
	s_cselect_b64 s[26:27], -1, 0
	s_and_b64 s[26:27], vcc, s[26:27]
	s_cmp_eq_u32 s28, 2
	v_cndmask_b32_e64 v14, v14, v25, s[26:27]
	s_cselect_b64 s[26:27], -1, 0
	s_and_b64 s[26:27], vcc, s[26:27]
	s_cmp_eq_u32 s28, 3
	v_cndmask_b32_e64 v15, v15, v25, s[26:27]
	s_cselect_b64 s[26:27], -1, 0
	s_and_b64 vcc, vcc, s[26:27]
	v_cndmask_b32_e32 v0, v0, v25, vcc
	v_max_f32_e32 v16, v0, v0
	v_max_f32_e32 v17, v15, v15
	v_max_f32_e32 v16, v17, v16
	v_max3_f32 v16, v9, v14, v16
	s_nop 1
	v_max_f32_dpp v16, v16, v16 quad_perm:[1,0,3,2] row_mask:0xf bank_mask:0xf bound_ctrl:1
	s_nop 1
	v_max_f32_dpp v16, v16, v16 quad_perm:[2,3,0,1] row_mask:0xf bank_mask:0xf bound_ctrl:1
	s_nop 1
	v_max_f32_dpp v16, v16, v16 row_half_mirror row_mask:0xf bank_mask:0xf bound_ctrl:1
	s_nop 1
	v_max_f32_dpp v16, v16, v16 row_mirror row_mask:0xf bank_mask:0xf bound_ctrl:1
	v_mov_b32_e32 v17, v16
	v_mov_b32_e32 v60, v16
	s_nop 1
	v_permlane16_swap_b32 v17, v60
	v_max_f32_e32 v16, v17, v60
	v_mov_b32_e32 v17, v16
	v_mov_b32_e32 v60, v16
	s_nop 1
	v_permlane32_swap_b32 v17, v60
	v_max_f32_e32 v16, v17, v60
	v_cmp_eq_f32_e32 vcc, v9, v16
	v_cmp_eq_f32_e64 s[28:29], v14, v16
	v_cmp_eq_f32_e64 s[26:27], v15, v16
	v_cmp_eq_f32_e64 s[38:39], v0, v16
	s_cbranch_vccz .LBB0_2223
	s_ff1_i32_b64 s54, vcc
	s_cbranch_execz .LBB0_2224
	s_branch .LBB0_2230

.LBB0_2230:
	s_and_b32 s26, s54, 63
	s_lshr_b32 s28, s54, 6
	s_cmp_lt_u32 s54, 64
	v_cmp_eq_u32_e32 vcc, s26, v22
	s_cselect_b64 s[26:27], -1, 0
	s_and_b64 s[26:27], s[26:27], vcc
	s_cmp_eq_u32 s28, 1
	v_cndmask_b32_e64 v9, v9, v25, s[26:27]
	s_cselect_b64 s[26:27], -1, 0
	s_and_b64 s[26:27], vcc, s[26:27]
	s_cmp_eq_u32 s28, 2
	v_cndmask_b32_e64 v14, v14, v25, s[26:27]
	s_cselect_b64 s[26:27], -1, 0
	s_and_b64 s[26:27], vcc, s[26:27]
	s_cmp_eq_u32 s28, 3
	v_cndmask_b32_e64 v15, v15, v25, s[26:27]
	s_cselect_b64 s[26:27], -1, 0
	s_and_b64 vcc, vcc, s[26:27]
	v_cndmask_b32_e32 v0, v0, v25, vcc
	v_max_f32_e32 v16, v0, v0
	v_max_f32_e32 v17, v15, v15
	v_max_f32_e32 v16, v17, v16
	v_max3_f32 v16, v9, v14, v16
	s_nop 1
	v_max_f32_dpp v16, v16, v16 quad_perm:[1,0,3,2] row_mask:0xf bank_mask:0xf bound_ctrl:1
	s_nop 1
	v_max_f32_dpp v16, v16, v16 quad_perm:[2,3,0,1] row_mask:0xf bank_mask:0xf bound_ctrl:1
	s_nop 1
	v_max_f32_dpp v16, v16, v16 row_half_mirror row_mask:0xf bank_mask:0xf bound_ctrl:1
	s_nop 1
	v_max_f32_dpp v16, v16, v16 row_mirror row_mask:0xf bank_mask:0xf bound_ctrl:1
	v_mov_b32_e32 v17, v16
	v_mov_b32_e32 v60, v16
	s_nop 1
	v_permlane16_swap_b32 v17, v60
	v_max_f32_e32 v16, v17, v60
	v_mov_b32_e32 v17, v16
	v_mov_b32_e32 v60, v16
	s_nop 1
	v_permlane32_swap_b32 v17, v60
	v_max_f32_e32 v16, v17, v60
	v_cmp_eq_f32_e32 vcc, v9, v16
	v_cmp_eq_f32_e64 s[28:29], v14, v16
	v_cmp_eq_f32_e64 s[26:27], v15, v16
	v_cmp_eq_f32_e64 s[38:39], v0, v16
	s_cbranch_vccz .LBB0_2232
	s_ff1_i32_b64 s55, vcc
	s_cbranch_execz .LBB0_2233
	s_branch .LBB0_2239
